# speedup vs baseline: 1.0803x; 1.0047x over previous
_Z5k_decPKiPKDF16_S2_PKfS4_S4_Pf:
	s_load_dword s3, s[0:1], 0x44
	s_load_dword s6, s[0:1], 0x38
	s_load_dwordx2 s[4:5], s[0:1], 0x0
	s_load_dwordx8 s[28:35], s[0:1], 0x8
	s_load_dwordx4 s[12:15], s[0:1], 0x28
	v_and_b32_e32 v1, 15, v0
	v_and_b32_e32 v64, 63, v0
	v_lshlrev_b32_e32 v96, 3, v1
	v_lshrrev_b32_e32 v4, 3, v0
	v_and_b32_e32 v4, 4, v4
	v_or_b32_e32 v96, v96, v4
	v_mov_b32_e32 v97, 0
	v_and_b32_e32 v104, 16, v0
	v_lshlrev_b32_e32 v6, 7, v0
	v_lshlrev_b32_e32 v7, 2, v64
	s_movk_i32 s16, 0x6000
	v_and_or_b32 v103, v6, s16, v7
	v_mov_b32_e32 v219, 0
	s_movk_i32 s19, 0x3d08
	s_waitcnt lgkmcnt(0)
	s_and_b32 s3, s3, 0xffff
	s_mul_i32 s2, s2, s3
	v_add_u32_e32 v5, s2, v0
	s_mul_i32 s6, s6, s3
	v_lshrrev_b32_e32 v102, 6, v5
	s_lshr_b32 s18, s6, 6
	v_readfirstlane_b32 s23, v102
	v_lshl_add_u64 v[2:3], s[4:5], 0, v[96:97]
	s_mov_b32 s16, 0xf4240
	v_cmp_gt_u32_e32 vcc, s16, v5
	s_and_saveexec_b64 s[22:23], vcc
	s_cbranch_execz .LBB2_3
	v_mov_b32_e32 v222, v2
	v_mov_b32_e32 v223, v3
	v_min_u32_e32 v218, s19, v102
	v_lshlrev_b32_e32 v218, 9, v218
	v_lshl_add_u64 v[216:217], v[222:223], 0, v[218:219]
	global_load_dword v65, v[216:217], off nt
	global_load_dword v80, v[216:217], off offset:128 nt
	global_load_dword v81, v[216:217], off offset:256 nt
	global_load_dword v82, v[216:217], off offset:384 nt
	v_add_u32_e32 v220, s18, v102
	v_min_u32_e32 v218, s19, v220
	v_lshlrev_b32_e32 v218, 9, v218
	v_lshl_add_u64 v[216:217], v[222:223], 0, v[218:219]
	global_load_dword v100, v[216:217], off nt
	global_load_dword v101, v[216:217], off offset:128 nt
	global_load_dword v98, v[216:217], off offset:256 nt
	global_load_dword v99, v[216:217], off offset:384 nt
	s_mov_b32 s8, s28
	s_and_b32 s9, s29, 0xffff
	s_mov_b32 s10, 0x30d400
	s_mov_b32 s11, 0x20000
	s_mov_b64 s[36:37], 0x1000
	v_and_b32_e32 v96, 48, v64
	v_lshlrev_b32_e32 v221, 6, v1
	v_lshlrev_b32_e32 v211, 2, v1
	v_mov_b32_e32 v214, v221
	v_mov_b32_e32 v215, 0
	v_lshl_add_u64 v[216:217], s[30:31], 0, v[96:97]
	v_lshl_add_u64 v[48:49], v[216:217], 0, v[214:215]
	v_lshl_add_u64 v[66:67], v[48:49], 0, s[36:37]
	v_lshl_or_b32 v221, v102, 6, v64
	v_lshrrev_b32_e32 v213, 4, v64
	v_cmp_gt_u32_e32 vcc, 16, v64
	global_load_dwordx4 v[68:71], v96, s[34:35]
	global_load_dwordx4 v[0:3], v96, s[32:33]
	global_load_dwordx4 v[72:75], v96, s[34:35] offset:64
	global_load_dwordx4 v[4:7], v96, s[32:33] offset:64
	global_load_dwordx4 v[76:79], v96, s[34:35] offset:128
	global_load_dwordx4 v[8:11], v96, s[32:33] offset:128
	global_load_dwordx4 v[106:109], v96, s[34:35] offset:192
	global_load_dwordx4 v[12:15], v96, s[32:33] offset:192
	global_load_dwordx4 v[110:113], v96, s[34:35] offset:256
	global_load_dwordx4 v[16:19], v96, s[32:33] offset:256
	global_load_dwordx4 v[114:117], v96, s[34:35] offset:320
	global_load_dwordx4 v[20:23], v96, s[32:33] offset:320
	global_load_dwordx4 v[118:121], v96, s[34:35] offset:384
	global_load_dwordx4 v[24:27], v96, s[32:33] offset:384
	global_load_dwordx4 v[122:125], v96, s[34:35] offset:448
	global_load_dwordx4 v[28:31], v96, s[32:33] offset:448
	global_load_dwordx4 v[32:35], v[48:49], off
	global_load_dwordx4 v[36:39], v[48:49], off offset:1024
	global_load_dwordx4 v[40:43], v[48:49], off offset:2048
	global_load_dwordx4 v[44:47], v[48:49], off offset:3072
	s_nop 0
	global_load_dwordx4 v[48:51], v[66:67], off
	global_load_dwordx4 v[52:55], v[66:67], off offset:1024
	global_load_dwordx4 v[56:59], v[66:67], off offset:2048
	global_load_dwordx4 v[60:63], v[66:67], off offset:3072
	global_load_dword v148, v211, s[34:35]
	global_load_dword v156, v211, s[32:33]
	global_load_dword v149, v211, s[34:35] offset:64
	global_load_dword v157, v211, s[32:33] offset:64
	global_load_dword v150, v211, s[34:35] offset:128
	global_load_dword v158, v211, s[32:33] offset:128
	global_load_dword v151, v211, s[34:35] offset:192
	global_load_dword v159, v211, s[32:33] offset:192
	global_load_dword v152, v211, s[34:35] offset:256
	global_load_dword v160, v211, s[32:33] offset:256
	global_load_dword v153, v211, s[34:35] offset:320
	global_load_dword v161, v211, s[32:33] offset:320
	global_load_dword v154, v211, s[34:35] offset:384
	global_load_dword v162, v211, s[32:33] offset:384
	global_load_dword v155, v211, s[34:35] offset:448
	global_load_dword v163, v211, s[32:33] offset:448
	s_load_dword s12, s[12:13], 0x0
	s_waitcnt vmcnt(44)
	v_lshl_or_b32 v216, v65, 5, v104
	v_lshl_or_b32 v217, v80, 5, v104
	v_lshl_or_b32 v218, v81, 5, v104
	v_lshl_or_b32 v212, v82, 5, v104
	buffer_load_dwordx4 v[92:95], v216, s[8:11], 0 offen
	buffer_load_dwordx4 v[88:91], v217, s[8:11], 0 offen
	buffer_load_dwordx4 v[84:87], v218, s[8:11], 0 offen
	buffer_load_dwordx4 v[80:83], v212, s[8:11], 0 offen
	s_lshl_b32 s21, s18, 6
	s_mov_b32 s20, 2
	s_mov_b64 s[16:17], 0
	v_cmp_eq_u32_e64 s[0:1], 1, v213
	v_cmp_eq_u32_e64 s[2:3], 2, v213
	v_cmp_eq_u32_e64 s[4:5], 3, v213
	v_mov_b32_e32 v96, v221
	v_mov_b32_e32 v97, 0
	s_waitcnt vmcnt(4)
	v_cvt_pk_f16_f32 v67, v74, v75
	v_cvt_pk_f16_f32 v66, v72, v73
	v_cvt_pk_f16_f32 v65, v70, v71
	v_cvt_pk_f16_f32 v64, v68, v69
	v_cvt_pk_f16_f32 v71, v108, v109
	v_cvt_pk_f16_f32 v70, v106, v107
	v_cvt_pk_f16_f32 v69, v78, v79
	v_cvt_pk_f16_f32 v68, v76, v77
	v_cvt_pk_f16_f32 v75, v116, v117
	v_cvt_pk_f16_f32 v74, v114, v115
	v_cvt_pk_f16_f32 v73, v112, v113
	v_cvt_pk_f16_f32 v72, v110, v111
	v_cvt_pk_f16_f32 v79, v124, v125
	v_cvt_pk_f16_f32 v78, v122, v123
	v_cvt_pk_f16_f32 v77, v120, v121
	v_cvt_pk_f16_f32 v76, v118, v119
	v_mov_b32_e32 v167, 0x38003800
	v_pk_mul_f16 v64, v64, v167
	v_pk_mul_f16 v65, v65, v167
	v_pk_mul_f16 v66, v66, v167
	v_pk_mul_f16 v67, v67, v167
	v_pk_mul_f16 v68, v68, v167
	v_pk_mul_f16 v69, v69, v167
	v_pk_mul_f16 v70, v70, v167
	v_pk_mul_f16 v71, v71, v167
	v_pk_mul_f16 v72, v72, v167
	v_pk_mul_f16 v73, v73, v167
	v_pk_mul_f16 v74, v74, v167
	v_pk_mul_f16 v75, v75, v167
	v_pk_mul_f16 v76, v76, v167
	v_pk_mul_f16 v77, v77, v167
	v_pk_mul_f16 v78, v78, v167
	v_pk_mul_f16 v79, v79, v167
	v_cvt_f16_f32_e32 v148, v148
	v_cvt_f16_f32_e32 v149, v149
	v_cvt_f16_f32_e32 v150, v150
	v_cvt_f16_f32_e32 v151, v151
	v_cvt_f16_f32_e32 v152, v152
	v_cvt_f16_f32_e32 v153, v153
	v_cvt_f16_f32_e32 v154, v154
	v_cvt_f16_f32_e32 v155, v155
	v_cvt_f32_f16_e32 v148, v148
	v_cvt_f32_f16_e32 v149, v149
	v_cvt_f32_f16_e32 v150, v150
	v_cvt_f32_f16_e32 v151, v151
	v_cvt_f32_f16_e32 v152, v152
	v_cvt_f32_f16_e32 v153, v153
	v_cvt_f32_f16_e32 v154, v154
	v_cvt_f32_f16_e32 v155, v155
	v_mul_f32_e32 v148, 0.5, v148
	v_mul_f32_e32 v149, 0.5, v149
	v_mul_f32_e32 v150, 0.5, v150
	v_mul_f32_e32 v151, 0.5, v151
	v_mul_f32_e32 v152, 0.5, v152
	v_mul_f32_e32 v153, 0.5, v153
	v_mul_f32_e32 v154, 0.5, v154
	v_mul_f32_e32 v155, 0.5, v155
	v_mov_b32_e32 v140, 0
	v_mov_b32_e32 v141, 0
	v_mov_b32_e32 v142, 0
	v_mov_b32_e32 v143, 0
	v_mov_b32_e32 v144, 0
	v_mov_b32_e32 v145, 0
	v_mov_b32_e32 v146, 0
	v_mov_b32_e32 v147, 0
	v_mov_b32_e32 v166, 0
	v_cvt_f32_f16_e32 v164, v32
	v_cvt_f32_f16_sdwa v165, v32 dst_sel:DWORD dst_unused:UNUSED_PAD src0_sel:WORD_1
	v_fmac_f32_e32 v140, v148, v164
	v_fmac_f32_e32 v141, v148, v165
	v_cvt_f32_f16_e32 v164, v33
	v_cvt_f32_f16_sdwa v165, v33 dst_sel:DWORD dst_unused:UNUSED_PAD src0_sel:WORD_1
	v_fmac_f32_e32 v142, v148, v164
	v_fmac_f32_e32 v143, v148, v165
	v_cvt_f32_f16_e32 v164, v34
	v_cvt_f32_f16_sdwa v165, v34 dst_sel:DWORD dst_unused:UNUSED_PAD src0_sel:WORD_1
	v_fmac_f32_e32 v144, v148, v164
	v_fmac_f32_e32 v145, v148, v165
	v_cvt_f32_f16_e32 v164, v35
	v_cvt_f32_f16_sdwa v165, v35 dst_sel:DWORD dst_unused:UNUSED_PAD src0_sel:WORD_1
	v_fmac_f32_e32 v146, v148, v164
	v_fmac_f32_e32 v147, v148, v165
	v_fmac_f32_e32 v166, v148, v156
	v_cvt_f32_f16_e32 v164, v36
	v_cvt_f32_f16_sdwa v165, v36 dst_sel:DWORD dst_unused:UNUSED_PAD src0_sel:WORD_1
	v_fmac_f32_e32 v140, v149, v164
	v_fmac_f32_e32 v141, v149, v165
	v_cvt_f32_f16_e32 v164, v37
	v_cvt_f32_f16_sdwa v165, v37 dst_sel:DWORD dst_unused:UNUSED_PAD src0_sel:WORD_1
	v_fmac_f32_e32 v142, v149, v164
	v_fmac_f32_e32 v143, v149, v165
	v_cvt_f32_f16_e32 v164, v38
	v_cvt_f32_f16_sdwa v165, v38 dst_sel:DWORD dst_unused:UNUSED_PAD src0_sel:WORD_1
	v_fmac_f32_e32 v144, v149, v164
	v_fmac_f32_e32 v145, v149, v165
	v_cvt_f32_f16_e32 v164, v39
	v_cvt_f32_f16_sdwa v165, v39 dst_sel:DWORD dst_unused:UNUSED_PAD src0_sel:WORD_1
	v_fmac_f32_e32 v146, v149, v164
	v_fmac_f32_e32 v147, v149, v165
	v_fmac_f32_e32 v166, v149, v157
	v_cvt_f32_f16_e32 v164, v40
	v_cvt_f32_f16_sdwa v165, v40 dst_sel:DWORD dst_unused:UNUSED_PAD src0_sel:WORD_1
	v_fmac_f32_e32 v140, v150, v164
	v_fmac_f32_e32 v141, v150, v165
	v_cvt_f32_f16_e32 v164, v41
	v_cvt_f32_f16_sdwa v165, v41 dst_sel:DWORD dst_unused:UNUSED_PAD src0_sel:WORD_1
	v_fmac_f32_e32 v142, v150, v164
	v_fmac_f32_e32 v143, v150, v165
	v_cvt_f32_f16_e32 v164, v42
	v_cvt_f32_f16_sdwa v165, v42 dst_sel:DWORD dst_unused:UNUSED_PAD src0_sel:WORD_1
	v_fmac_f32_e32 v144, v150, v164
	v_fmac_f32_e32 v145, v150, v165
	v_cvt_f32_f16_e32 v164, v43
	v_cvt_f32_f16_sdwa v165, v43 dst_sel:DWORD dst_unused:UNUSED_PAD src0_sel:WORD_1
	v_fmac_f32_e32 v146, v150, v164
	v_fmac_f32_e32 v147, v150, v165
	v_fmac_f32_e32 v166, v150, v158
	v_cvt_f32_f16_e32 v164, v44
	v_cvt_f32_f16_sdwa v165, v44 dst_sel:DWORD dst_unused:UNUSED_PAD src0_sel:WORD_1
	v_fmac_f32_e32 v140, v151, v164
	v_fmac_f32_e32 v141, v151, v165
	v_cvt_f32_f16_e32 v164, v45
	v_cvt_f32_f16_sdwa v165, v45 dst_sel:DWORD dst_unused:UNUSED_PAD src0_sel:WORD_1
	v_fmac_f32_e32 v142, v151, v164
	v_fmac_f32_e32 v143, v151, v165
	v_cvt_f32_f16_e32 v164, v46
	v_cvt_f32_f16_sdwa v165, v46 dst_sel:DWORD dst_unused:UNUSED_PAD src0_sel:WORD_1
	v_fmac_f32_e32 v144, v151, v164
	v_fmac_f32_e32 v145, v151, v165
	v_cvt_f32_f16_e32 v164, v47
	v_cvt_f32_f16_sdwa v165, v47 dst_sel:DWORD dst_unused:UNUSED_PAD src0_sel:WORD_1
	v_fmac_f32_e32 v146, v151, v164
	v_fmac_f32_e32 v147, v151, v165
	v_fmac_f32_e32 v166, v151, v159
	v_cvt_f32_f16_e32 v164, v48
	v_cvt_f32_f16_sdwa v165, v48 dst_sel:DWORD dst_unused:UNUSED_PAD src0_sel:WORD_1
	v_fmac_f32_e32 v140, v152, v164
	v_fmac_f32_e32 v141, v152, v165
	v_cvt_f32_f16_e32 v164, v49
	v_cvt_f32_f16_sdwa v165, v49 dst_sel:DWORD dst_unused:UNUSED_PAD src0_sel:WORD_1
	v_fmac_f32_e32 v142, v152, v164
	v_fmac_f32_e32 v143, v152, v165
	v_cvt_f32_f16_e32 v164, v50
	v_cvt_f32_f16_sdwa v165, v50 dst_sel:DWORD dst_unused:UNUSED_PAD src0_sel:WORD_1
	v_fmac_f32_e32 v144, v152, v164
	v_fmac_f32_e32 v145, v152, v165
	v_cvt_f32_f16_e32 v164, v51
	v_cvt_f32_f16_sdwa v165, v51 dst_sel:DWORD dst_unused:UNUSED_PAD src0_sel:WORD_1
	v_fmac_f32_e32 v146, v152, v164
	v_fmac_f32_e32 v147, v152, v165
	v_fmac_f32_e32 v166, v152, v160
	v_cvt_f32_f16_e32 v164, v52
	v_cvt_f32_f16_sdwa v165, v52 dst_sel:DWORD dst_unused:UNUSED_PAD src0_sel:WORD_1
	v_fmac_f32_e32 v140, v153, v164
	v_fmac_f32_e32 v141, v153, v165
	v_cvt_f32_f16_e32 v164, v53
	v_cvt_f32_f16_sdwa v165, v53 dst_sel:DWORD dst_unused:UNUSED_PAD src0_sel:WORD_1
	v_fmac_f32_e32 v142, v153, v164
	v_fmac_f32_e32 v143, v153, v165
	v_cvt_f32_f16_e32 v164, v54
	v_cvt_f32_f16_sdwa v165, v54 dst_sel:DWORD dst_unused:UNUSED_PAD src0_sel:WORD_1
	v_fmac_f32_e32 v144, v153, v164
	v_fmac_f32_e32 v145, v153, v165
	v_cvt_f32_f16_e32 v164, v55
	v_cvt_f32_f16_sdwa v165, v55 dst_sel:DWORD dst_unused:UNUSED_PAD src0_sel:WORD_1
	v_fmac_f32_e32 v146, v153, v164
	v_fmac_f32_e32 v147, v153, v165
	v_fmac_f32_e32 v166, v153, v161
	v_cvt_f32_f16_e32 v164, v56
	v_cvt_f32_f16_sdwa v165, v56 dst_sel:DWORD dst_unused:UNUSED_PAD src0_sel:WORD_1
	v_fmac_f32_e32 v140, v154, v164
	v_fmac_f32_e32 v141, v154, v165
	v_cvt_f32_f16_e32 v164, v57
	v_cvt_f32_f16_sdwa v165, v57 dst_sel:DWORD dst_unused:UNUSED_PAD src0_sel:WORD_1
	v_fmac_f32_e32 v142, v154, v164
	v_fmac_f32_e32 v143, v154, v165
	v_cvt_f32_f16_e32 v164, v58
	v_cvt_f32_f16_sdwa v165, v58 dst_sel:DWORD dst_unused:UNUSED_PAD src0_sel:WORD_1
	v_fmac_f32_e32 v144, v154, v164
	v_fmac_f32_e32 v145, v154, v165
	v_cvt_f32_f16_e32 v164, v59
	v_cvt_f32_f16_sdwa v165, v59 dst_sel:DWORD dst_unused:UNUSED_PAD src0_sel:WORD_1
	v_fmac_f32_e32 v146, v154, v164
	v_fmac_f32_e32 v147, v154, v165
	v_fmac_f32_e32 v166, v154, v162
	v_cvt_f32_f16_e32 v164, v60
	v_cvt_f32_f16_sdwa v165, v60 dst_sel:DWORD dst_unused:UNUSED_PAD src0_sel:WORD_1
	v_fmac_f32_e32 v140, v155, v164
	v_fmac_f32_e32 v141, v155, v165
	v_cvt_f32_f16_e32 v164, v61
	v_cvt_f32_f16_sdwa v165, v61 dst_sel:DWORD dst_unused:UNUSED_PAD src0_sel:WORD_1
	v_fmac_f32_e32 v142, v155, v164
	v_fmac_f32_e32 v143, v155, v165
	v_cvt_f32_f16_e32 v164, v62
	v_cvt_f32_f16_sdwa v165, v62 dst_sel:DWORD dst_unused:UNUSED_PAD src0_sel:WORD_1
	v_fmac_f32_e32 v144, v155, v164
	v_fmac_f32_e32 v145, v155, v165
	v_cvt_f32_f16_e32 v164, v63
	v_cvt_f32_f16_sdwa v165, v63 dst_sel:DWORD dst_unused:UNUSED_PAD src0_sel:WORD_1
	v_fmac_f32_e32 v146, v155, v164
	v_fmac_f32_e32 v147, v155, v165
	v_fmac_f32_e32 v166, v155, v163
	v_add_f32_dpp v140, v140, v140 row_ror:8 row_mask:0xf bank_mask:0xf
	v_add_f32_dpp v141, v141, v141 row_ror:8 row_mask:0xf bank_mask:0xf
	v_add_f32_dpp v142, v142, v142 row_ror:8 row_mask:0xf bank_mask:0xf
	v_add_f32_dpp v143, v143, v143 row_ror:8 row_mask:0xf bank_mask:0xf
	v_add_f32_dpp v144, v144, v144 row_ror:8 row_mask:0xf bank_mask:0xf
	v_add_f32_dpp v145, v145, v145 row_ror:8 row_mask:0xf bank_mask:0xf
	v_add_f32_dpp v146, v146, v146 row_ror:8 row_mask:0xf bank_mask:0xf
	v_add_f32_dpp v147, v147, v147 row_ror:8 row_mask:0xf bank_mask:0xf
	v_add_f32_dpp v166, v166, v166 row_ror:8 row_mask:0xf bank_mask:0xf
	v_add_f32_dpp v140, v140, v140 row_ror:4 row_mask:0xf bank_mask:0xf
	v_add_f32_dpp v141, v141, v141 row_ror:4 row_mask:0xf bank_mask:0xf
	v_add_f32_dpp v142, v142, v142 row_ror:4 row_mask:0xf bank_mask:0xf
	v_add_f32_dpp v143, v143, v143 row_ror:4 row_mask:0xf bank_mask:0xf
	v_add_f32_dpp v144, v144, v144 row_ror:4 row_mask:0xf bank_mask:0xf
	v_add_f32_dpp v145, v145, v145 row_ror:4 row_mask:0xf bank_mask:0xf
	v_add_f32_dpp v146, v146, v146 row_ror:4 row_mask:0xf bank_mask:0xf
	v_add_f32_dpp v147, v147, v147 row_ror:4 row_mask:0xf bank_mask:0xf
	v_add_f32_dpp v166, v166, v166 row_ror:4 row_mask:0xf bank_mask:0xf
	v_add_f32_dpp v140, v140, v140 row_ror:2 row_mask:0xf bank_mask:0xf
	v_add_f32_dpp v141, v141, v141 row_ror:2 row_mask:0xf bank_mask:0xf
	v_add_f32_dpp v142, v142, v142 row_ror:2 row_mask:0xf bank_mask:0xf
	v_add_f32_dpp v143, v143, v143 row_ror:2 row_mask:0xf bank_mask:0xf
	v_add_f32_dpp v144, v144, v144 row_ror:2 row_mask:0xf bank_mask:0xf
	v_add_f32_dpp v145, v145, v145 row_ror:2 row_mask:0xf bank_mask:0xf
	v_add_f32_dpp v146, v146, v146 row_ror:2 row_mask:0xf bank_mask:0xf
	v_add_f32_dpp v147, v147, v147 row_ror:2 row_mask:0xf bank_mask:0xf
	v_add_f32_dpp v166, v166, v166 row_ror:2 row_mask:0xf bank_mask:0xf
	v_add_f32_dpp v140, v140, v140 row_ror:1 row_mask:0xf bank_mask:0xf
	v_add_f32_dpp v141, v141, v141 row_ror:1 row_mask:0xf bank_mask:0xf
	v_add_f32_dpp v142, v142, v142 row_ror:1 row_mask:0xf bank_mask:0xf
	v_add_f32_dpp v143, v143, v143 row_ror:1 row_mask:0xf bank_mask:0xf
	v_add_f32_dpp v144, v144, v144 row_ror:1 row_mask:0xf bank_mask:0xf
	v_add_f32_dpp v145, v145, v145 row_ror:1 row_mask:0xf bank_mask:0xf
	v_add_f32_dpp v146, v146, v146 row_ror:1 row_mask:0xf bank_mask:0xf
	v_add_f32_dpp v147, v147, v147 row_ror:1 row_mask:0xf bank_mask:0xf
	v_add_f32_dpp v166, v166, v166 row_ror:1 row_mask:0xf bank_mask:0xf
	v_cvt_pk_f16_f32 v252, v140, v141
	v_cvt_pk_f16_f32 v253, v142, v143
	v_cvt_pk_f16_f32 v254, v144, v145
	v_cvt_pk_f16_f32 v255, v146, v147
	s_waitcnt lgkmcnt(0)
	v_add_f32_e32 v209, s12, v166
	v_add_u32_e32 v220, s18, v102
	v_add_u32_e32 v220, s18, v220
	v_min_u32_e32 v218, s19, v220
	v_lshlrev_b32_e32 v218, 9, v218
	v_lshl_add_u64 v[216:217], v[222:223], 0, v[218:219]
	global_load_dword v228, v[216:217], off nt
	global_load_dword v229, v[216:217], off offset:128 nt
	global_load_dword v230, v[216:217], off offset:256 nt
	global_load_dword v231, v[216:217], off offset:384 nt
	v_add_u32_e32 v220, s18, v220
	v_min_u32_e32 v218, s19, v220
	v_lshlrev_b32_e32 v218, 9, v218
	v_lshl_add_u64 v[216:217], v[222:223], 0, v[218:219]
	global_load_dword v232, v[216:217], off nt
	global_load_dword v233, v[216:217], off offset:128 nt
	global_load_dword v234, v[216:217], off offset:256 nt
	global_load_dword v235, v[216:217], off offset:384 nt
	v_add_u32_e32 v220, s18, v220
	v_min_u32_e32 v218, s19, v220
	v_lshlrev_b32_e32 v218, 9, v218
	v_lshl_add_u64 v[216:217], v[222:223], 0, v[218:219]
	global_load_dword v236, v[216:217], off nt
	global_load_dword v237, v[216:217], off offset:128 nt
	global_load_dword v238, v[216:217], off offset:256 nt
	global_load_dword v239, v[216:217], off offset:384 nt
	v_add_u32_e32 v220, s18, v220
	v_min_u32_e32 v218, s19, v220
	v_lshlrev_b32_e32 v218, 9, v218
	v_lshl_add_u64 v[216:217], v[222:223], 0, v[218:219]
	global_load_dword v240, v[216:217], off nt
	global_load_dword v241, v[216:217], off offset:128 nt
	global_load_dword v242, v[216:217], off offset:256 nt
	global_load_dword v243, v[216:217], off offset:384 nt
	v_add_u32_e32 v220, s18, v220
	v_min_u32_e32 v218, s19, v220
	v_lshlrev_b32_e32 v218, 9, v218
	v_lshl_add_u64 v[216:217], v[222:223], 0, v[218:219]
	global_load_dword v244, v[216:217], off nt
	global_load_dword v245, v[216:217], off offset:128 nt
	global_load_dword v246, v[216:217], off offset:256 nt
	global_load_dword v247, v[216:217], off offset:384 nt
	v_add_u32_e32 v220, s18, v220
	v_min_u32_e32 v218, s19, v220
	v_lshlrev_b32_e32 v218, 9, v218
	v_lshl_add_u64 v[216:217], v[222:223], 0, v[218:219]
	global_load_dword v248, v[216:217], off nt
	global_load_dword v249, v[216:217], off offset:128 nt
	global_load_dword v250, v[216:217], off offset:256 nt
	global_load_dword v251, v[216:217], off offset:384 nt
	s_waitcnt vmcnt(24)
.LBB2_2:
	s_min_i32 s6, s20, 7
	s_add_i32 s20, s20, 1
	s_add_u32 s24, s23, s18
	s_cmp_gt_u32 s24, s19
	s_cselect_b32 s22, 0x40000000, 0
	v_lshl_or_b32 v204, v100, 5, v104
	v_lshl_or_b32 v205, v101, 5, v104
	v_lshl_or_b32 v206, v98, 5, v104
	v_lshl_or_b32 v207, v99, 5, v104
	buffer_load_dwordx4 v[212:215], v204, s[8:11], s22 offen
	buffer_load_dwordx4 v[216:219], v205, s[8:11], s22 offen
	buffer_load_dwordx4 v[220:223], v206, s[8:11], s22 offen
	buffer_load_dwordx4 v[224:227], v207, s[8:11], s22 offen
	v_lshl_add_u64 v[106:107], v[96:97], 2, s[14:15]
	v_lshl_add_u32 v105, s6, 10, v103
	v_add_u32_e32 v96, s21, v96
	v_mfma_f32_16x16x32_f16 v[108:111], v[32:35], v[92:95], v[0:3]
	v_mfma_f32_16x16x32_f16 v[112:115], v[36:39], v[92:95], v[4:7]
	v_mfma_f32_16x16x32_f16 v[188:191], v[252:255], v[92:95], 0
	v_mfma_f32_16x16x32_f16 v[116:119], v[32:35], v[88:91], v[0:3]
	v_mfma_f32_16x16x32_f16 v[120:123], v[36:39], v[88:91], v[4:7]
	v_mfma_f32_16x16x32_f16 v[192:195], v[252:255], v[88:91], 0
	v_mfma_f32_16x16x32_f16 v[124:127], v[32:35], v[84:87], v[0:3]
	v_mfma_f32_16x16x32_f16 v[128:131], v[36:39], v[84:87], v[4:7]
	v_mfma_f32_16x16x32_f16 v[196:199], v[252:255], v[84:87], 0
	v_mfma_f32_16x16x32_f16 v[132:135], v[32:35], v[80:83], v[0:3]
	v_mfma_f32_16x16x32_f16 v[136:139], v[36:39], v[80:83], v[4:7]
	v_mfma_f32_16x16x32_f16 v[200:203], v[252:255], v[80:83], 0
	v_mfma_f32_16x16x32_f16 v[140:143], v[40:43], v[92:95], v[8:11]
	v_cvt_pk_f16_f32 v172, |v108|, |v109|
	v_cvt_pk_f16_f32 v173, |v110|, |v111|
	v_mfma_f32_16x16x32_f16 v[144:147], v[44:47], v[92:95], v[12:15]
	v_cvt_pk_f16_f32 v174, |v112|, |v113|
	v_cvt_pk_f16_f32 v175, |v114|, |v115|
	v_mfma_f32_16x16x32_f16 v[148:151], v[40:43], v[88:91], v[8:11]
	v_cvt_pk_f16_f32 v176, |v116|, |v117|
	v_cvt_pk_f16_f32 v177, |v118|, |v119|
	v_mfma_f32_16x16x32_f16 v[188:191], v[64:67], v[172:175], v[188:191]
	v_mfma_f32_16x16x32_f16 v[152:155], v[44:47], v[88:91], v[12:15]
	v_cvt_pk_f16_f32 v178, |v120|, |v121|
	v_cvt_pk_f16_f32 v179, |v122|, |v123|
	v_mfma_f32_16x16x32_f16 v[156:159], v[40:43], v[84:87], v[8:11]
	v_cvt_pk_f16_f32 v180, |v124|, |v125|
	v_cvt_pk_f16_f32 v181, |v126|, |v127|
	v_mfma_f32_16x16x32_f16 v[192:195], v[64:67], v[176:179], v[192:195]
	v_mfma_f32_16x16x32_f16 v[160:163], v[44:47], v[84:87], v[12:15]
	v_cvt_pk_f16_f32 v182, |v128|, |v129|
	v_cvt_pk_f16_f32 v183, |v130|, |v131|
	v_mfma_f32_16x16x32_f16 v[164:167], v[40:43], v[80:83], v[8:11]
	v_cvt_pk_f16_f32 v184, |v132|, |v133|
	v_cvt_pk_f16_f32 v185, |v134|, |v135|
	v_mfma_f32_16x16x32_f16 v[196:199], v[64:67], v[180:183], v[196:199]
	v_mfma_f32_16x16x32_f16 v[168:171], v[44:47], v[80:83], v[12:15]
	v_cvt_pk_f16_f32 v186, |v136|, |v137|
	v_cvt_pk_f16_f32 v187, |v138|, |v139|
	s_nop 1
	v_mfma_f32_16x16x32_f16 v[200:203], v[64:67], v[184:187], v[200:203]
	v_mfma_f32_16x16x32_f16 v[108:111], v[48:51], v[92:95], v[16:19]
	v_cvt_pk_f16_f32 v172, |v140|, |v141|
	v_cvt_pk_f16_f32 v173, |v142|, |v143|
	v_mfma_f32_16x16x32_f16 v[112:115], v[52:55], v[92:95], v[20:23]
	v_cvt_pk_f16_f32 v174, |v144|, |v145|
	v_cvt_pk_f16_f32 v175, |v146|, |v147|
	v_mfma_f32_16x16x32_f16 v[116:119], v[48:51], v[88:91], v[16:19]
	v_cvt_pk_f16_f32 v176, |v148|, |v149|
	v_cvt_pk_f16_f32 v177, |v150|, |v151|
	v_mfma_f32_16x16x32_f16 v[188:191], v[68:71], v[172:175], v[188:191]
	v_mfma_f32_16x16x32_f16 v[120:123], v[52:55], v[88:91], v[20:23]
	v_cvt_pk_f16_f32 v178, |v152|, |v153|
	v_cvt_pk_f16_f32 v179, |v154|, |v155|
	v_mfma_f32_16x16x32_f16 v[124:127], v[48:51], v[84:87], v[16:19]
	v_cvt_pk_f16_f32 v180, |v156|, |v157|
	v_cvt_pk_f16_f32 v181, |v158|, |v159|
	v_mfma_f32_16x16x32_f16 v[192:195], v[68:71], v[176:179], v[192:195]
	v_mfma_f32_16x16x32_f16 v[128:131], v[52:55], v[84:87], v[20:23]
	v_cvt_pk_f16_f32 v182, |v160|, |v161|
	v_cvt_pk_f16_f32 v183, |v162|, |v163|
	v_mfma_f32_16x16x32_f16 v[132:135], v[48:51], v[80:83], v[16:19]
	v_cvt_pk_f16_f32 v184, |v164|, |v165|
	v_cvt_pk_f16_f32 v185, |v166|, |v167|
	v_mfma_f32_16x16x32_f16 v[196:199], v[68:71], v[180:183], v[196:199]
	v_mfma_f32_16x16x32_f16 v[136:139], v[52:55], v[80:83], v[20:23]
	v_cvt_pk_f16_f32 v186, |v168|, |v169|
	v_cvt_pk_f16_f32 v187, |v170|, |v171|
	s_nop 1
	v_mfma_f32_16x16x32_f16 v[200:203], v[68:71], v[184:187], v[200:203]
	v_mfma_f32_16x16x32_f16 v[140:143], v[56:59], v[92:95], v[24:27]
	v_cvt_pk_f16_f32 v172, |v108|, |v109|
	v_cvt_pk_f16_f32 v173, |v110|, |v111|
	v_mfma_f32_16x16x32_f16 v[144:147], v[60:63], v[92:95], v[28:31]
	v_cvt_pk_f16_f32 v174, |v112|, |v113|
	v_cvt_pk_f16_f32 v175, |v114|, |v115|
	v_mfma_f32_16x16x32_f16 v[148:151], v[56:59], v[88:91], v[24:27]
	v_cvt_pk_f16_f32 v176, |v116|, |v117|
	v_cvt_pk_f16_f32 v177, |v118|, |v119|
	v_mfma_f32_16x16x32_f16 v[188:191], v[72:75], v[172:175], v[188:191]
	v_mfma_f32_16x16x32_f16 v[152:155], v[60:63], v[88:91], v[28:31]
	v_cvt_pk_f16_f32 v178, |v120|, |v121|
	v_cvt_pk_f16_f32 v179, |v122|, |v123|
	v_mfma_f32_16x16x32_f16 v[156:159], v[56:59], v[84:87], v[24:27]
	v_cvt_pk_f16_f32 v180, |v124|, |v125|
	v_cvt_pk_f16_f32 v181, |v126|, |v127|
	v_mfma_f32_16x16x32_f16 v[192:195], v[72:75], v[176:179], v[192:195]
	v_mfma_f32_16x16x32_f16 v[160:163], v[60:63], v[84:87], v[28:31]
	v_cvt_pk_f16_f32 v182, |v128|, |v129|
	v_cvt_pk_f16_f32 v183, |v130|, |v131|
	v_mfma_f32_16x16x32_f16 v[164:167], v[56:59], v[80:83], v[24:27]
	v_cvt_pk_f16_f32 v184, |v132|, |v133|
	v_cvt_pk_f16_f32 v185, |v134|, |v135|
	v_mfma_f32_16x16x32_f16 v[196:199], v[72:75], v[180:183], v[196:199]
	v_mfma_f32_16x16x32_f16 v[168:171], v[60:63], v[80:83], v[28:31]
	v_cvt_pk_f16_f32 v186, |v136|, |v137|
	v_cvt_pk_f16_f32 v187, |v138|, |v139|
	s_nop 1
	v_mfma_f32_16x16x32_f16 v[200:203], v[72:75], v[184:187], v[200:203]
	v_cvt_pk_f16_f32 v172, |v140|, |v141|
	v_cvt_pk_f16_f32 v173, |v142|, |v143|
	v_cvt_pk_f16_f32 v174, |v144|, |v145|
	v_cvt_pk_f16_f32 v175, |v146|, |v147|
	s_cmp_lg_u32 s20, 3
	s_cbranch_scc1 .Ldec_noidx_A
	s_waitcnt vmcnt(4)
	ds_write2st64_b32 v103, v228, v229 offset0:8 offset1:9
	ds_write2st64_b32 v103, v230, v231 offset0:10 offset1:11
	ds_write2st64_b32 v103, v232, v233 offset0:12 offset1:13
	ds_write2st64_b32 v103, v234, v235 offset0:14 offset1:15
	ds_write2st64_b32 v103, v236, v237 offset0:16 offset1:17
	ds_write2st64_b32 v103, v238, v239 offset0:18 offset1:19
	ds_write2st64_b32 v103, v240, v241 offset0:20 offset1:21
	ds_write2st64_b32 v103, v242, v243 offset0:22 offset1:23
	ds_write2st64_b32 v103, v244, v245 offset0:24 offset1:25
	ds_write2st64_b32 v103, v246, v247 offset0:26 offset1:27
	ds_write2st64_b32 v103, v248, v249 offset0:28 offset1:29
	ds_write2st64_b32 v103, v250, v251 offset0:30 offset1:31
.Ldec_noidx_A:
	v_cvt_pk_f16_f32 v176, |v148|, |v149|
	v_cvt_pk_f16_f32 v177, |v150|, |v151|
	v_cvt_pk_f16_f32 v178, |v152|, |v153|
	v_cvt_pk_f16_f32 v179, |v154|, |v155|
	v_mfma_f32_16x16x32_f16 v[188:191], v[76:79], v[172:175], v[188:191]
	ds_read2st64_b32 v[100:101], v105 offset1:1
	ds_read2st64_b32 v[98:99], v105 offset0:2 offset1:3
	v_cvt_pk_f16_f32 v180, |v156|, |v157|
	v_cvt_pk_f16_f32 v181, |v158|, |v159|
	v_cvt_pk_f16_f32 v182, |v160|, |v161|
	v_cvt_pk_f16_f32 v183, |v162|, |v163|
	v_mfma_f32_16x16x32_f16 v[192:195], v[76:79], v[176:179], v[192:195]
	v_cvt_pk_f16_f32 v184, |v164|, |v165|
	v_cvt_pk_f16_f32 v185, |v166|, |v167|
	v_cvt_pk_f16_f32 v186, |v168|, |v169|
	v_cvt_pk_f16_f32 v187, |v170|, |v171|
	v_mfma_f32_16x16x32_f16 v[196:199], v[76:79], v[180:183], v[196:199]
	s_nop 1
	v_mfma_f32_16x16x32_f16 v[200:203], v[76:79], v[184:187], v[200:203]
	s_mov_b32 s23, s24
	v_cndmask_b32_e32 v208, 0, v188, vcc
	s_nop 0
	v_cndmask_b32_e64 v208, v208, v192, s[0:1]
	s_nop 0
	v_cndmask_b32_e64 v208, v208, v196, s[2:3]
	s_nop 4
	v_cndmask_b32_e64 v208, v208, v200, s[4:5]
	s_waitcnt lgkmcnt(0)
	v_add_f32_e32 v208, v209, v208
	v_mul_f32_e32 v208, 0xbfb8aa3b, v208
	v_exp_f32_e32 v208, v208
	s_nop 0
	v_add_f32_e32 v208, 1.0, v208
	v_rcp_f32_e32 v208, v208
	s_nop 0
	global_store_dword v[106:107], v208, off sc0 sc1
	s_waitcnt vmcnt(1)
	s_cmp_le_u32 s23, s19
	s_cbranch_scc0 .LBB2_3
	s_min_i32 s6, s20, 7
	s_add_i32 s20, s20, 1
	s_add_u32 s24, s23, s18
	s_cmp_gt_u32 s24, s19
	s_cselect_b32 s22, 0x40000000, 0
	v_lshl_or_b32 v204, v100, 5, v104
	v_lshl_or_b32 v205, v101, 5, v104
	v_lshl_or_b32 v206, v98, 5, v104
	v_lshl_or_b32 v207, v99, 5, v104
	buffer_load_dwordx4 v[92:95], v204, s[8:11], s22 offen
	buffer_load_dwordx4 v[88:91], v205, s[8:11], s22 offen
	buffer_load_dwordx4 v[84:87], v206, s[8:11], s22 offen
	buffer_load_dwordx4 v[80:83], v207, s[8:11], s22 offen
	v_lshl_add_u64 v[106:107], v[96:97], 2, s[14:15]
	v_lshl_add_u32 v105, s6, 10, v103
	v_add_u32_e32 v96, s21, v96
	v_mfma_f32_16x16x32_f16 v[108:111], v[32:35], v[212:215], v[0:3]
	v_mfma_f32_16x16x32_f16 v[112:115], v[36:39], v[212:215], v[4:7]
	v_mfma_f32_16x16x32_f16 v[188:191], v[252:255], v[212:215], 0
	v_mfma_f32_16x16x32_f16 v[116:119], v[32:35], v[216:219], v[0:3]
	v_mfma_f32_16x16x32_f16 v[120:123], v[36:39], v[216:219], v[4:7]
	v_mfma_f32_16x16x32_f16 v[192:195], v[252:255], v[216:219], 0
	v_mfma_f32_16x16x32_f16 v[124:127], v[32:35], v[220:223], v[0:3]
	v_mfma_f32_16x16x32_f16 v[128:131], v[36:39], v[220:223], v[4:7]
	v_mfma_f32_16x16x32_f16 v[196:199], v[252:255], v[220:223], 0
	v_mfma_f32_16x16x32_f16 v[132:135], v[32:35], v[224:227], v[0:3]
	v_mfma_f32_16x16x32_f16 v[136:139], v[36:39], v[224:227], v[4:7]
	v_mfma_f32_16x16x32_f16 v[200:203], v[252:255], v[224:227], 0
	v_mfma_f32_16x16x32_f16 v[140:143], v[40:43], v[212:215], v[8:11]
	v_cvt_pk_f16_f32 v172, |v108|, |v109|
	v_cvt_pk_f16_f32 v173, |v110|, |v111|
	v_mfma_f32_16x16x32_f16 v[144:147], v[44:47], v[212:215], v[12:15]
	v_cvt_pk_f16_f32 v174, |v112|, |v113|
	v_cvt_pk_f16_f32 v175, |v114|, |v115|
	v_mfma_f32_16x16x32_f16 v[148:151], v[40:43], v[216:219], v[8:11]
	v_cvt_pk_f16_f32 v176, |v116|, |v117|
	v_cvt_pk_f16_f32 v177, |v118|, |v119|
	v_mfma_f32_16x16x32_f16 v[188:191], v[64:67], v[172:175], v[188:191]
	v_mfma_f32_16x16x32_f16 v[152:155], v[44:47], v[216:219], v[12:15]
	v_cvt_pk_f16_f32 v178, |v120|, |v121|
	v_cvt_pk_f16_f32 v179, |v122|, |v123|
	v_mfma_f32_16x16x32_f16 v[156:159], v[40:43], v[220:223], v[8:11]
	v_cvt_pk_f16_f32 v180, |v124|, |v125|
	v_cvt_pk_f16_f32 v181, |v126|, |v127|
	v_mfma_f32_16x16x32_f16 v[192:195], v[64:67], v[176:179], v[192:195]
	v_mfma_f32_16x16x32_f16 v[160:163], v[44:47], v[220:223], v[12:15]
	v_cvt_pk_f16_f32 v182, |v128|, |v129|
	v_cvt_pk_f16_f32 v183, |v130|, |v131|
	v_mfma_f32_16x16x32_f16 v[164:167], v[40:43], v[224:227], v[8:11]
	v_cvt_pk_f16_f32 v184, |v132|, |v133|
	v_cvt_pk_f16_f32 v185, |v134|, |v135|
	v_mfma_f32_16x16x32_f16 v[196:199], v[64:67], v[180:183], v[196:199]
	v_mfma_f32_16x16x32_f16 v[168:171], v[44:47], v[224:227], v[12:15]
	v_cvt_pk_f16_f32 v186, |v136|, |v137|
	v_cvt_pk_f16_f32 v187, |v138|, |v139|
	s_nop 1
	v_mfma_f32_16x16x32_f16 v[200:203], v[64:67], v[184:187], v[200:203]
	v_mfma_f32_16x16x32_f16 v[108:111], v[48:51], v[212:215], v[16:19]
	v_cvt_pk_f16_f32 v172, |v140|, |v141|
	v_cvt_pk_f16_f32 v173, |v142|, |v143|
	v_mfma_f32_16x16x32_f16 v[112:115], v[52:55], v[212:215], v[20:23]
	v_cvt_pk_f16_f32 v174, |v144|, |v145|
	v_cvt_pk_f16_f32 v175, |v146|, |v147|
	v_mfma_f32_16x16x32_f16 v[116:119], v[48:51], v[216:219], v[16:19]
	v_cvt_pk_f16_f32 v176, |v148|, |v149|
	v_cvt_pk_f16_f32 v177, |v150|, |v151|
	v_mfma_f32_16x16x32_f16 v[188:191], v[68:71], v[172:175], v[188:191]
	v_mfma_f32_16x16x32_f16 v[120:123], v[52:55], v[216:219], v[20:23]
	v_cvt_pk_f16_f32 v178, |v152|, |v153|
	v_cvt_pk_f16_f32 v179, |v154|, |v155|
	v_mfma_f32_16x16x32_f16 v[124:127], v[48:51], v[220:223], v[16:19]
	v_cvt_pk_f16_f32 v180, |v156|, |v157|
	v_cvt_pk_f16_f32 v181, |v158|, |v159|
	v_mfma_f32_16x16x32_f16 v[192:195], v[68:71], v[176:179], v[192:195]
	v_mfma_f32_16x16x32_f16 v[128:131], v[52:55], v[220:223], v[20:23]
	v_cvt_pk_f16_f32 v182, |v160|, |v161|
	v_cvt_pk_f16_f32 v183, |v162|, |v163|
	v_mfma_f32_16x16x32_f16 v[132:135], v[48:51], v[224:227], v[16:19]
	v_cvt_pk_f16_f32 v184, |v164|, |v165|
	v_cvt_pk_f16_f32 v185, |v166|, |v167|
	v_mfma_f32_16x16x32_f16 v[196:199], v[68:71], v[180:183], v[196:199]
	v_mfma_f32_16x16x32_f16 v[136:139], v[52:55], v[224:227], v[20:23]
	v_cvt_pk_f16_f32 v186, |v168|, |v169|
	v_cvt_pk_f16_f32 v187, |v170|, |v171|
	s_nop 1
	v_mfma_f32_16x16x32_f16 v[200:203], v[68:71], v[184:187], v[200:203]
	v_mfma_f32_16x16x32_f16 v[140:143], v[56:59], v[212:215], v[24:27]
	v_cvt_pk_f16_f32 v172, |v108|, |v109|
	v_cvt_pk_f16_f32 v173, |v110|, |v111|
	v_mfma_f32_16x16x32_f16 v[144:147], v[60:63], v[212:215], v[28:31]
	v_cvt_pk_f16_f32 v174, |v112|, |v113|
	v_cvt_pk_f16_f32 v175, |v114|, |v115|
	v_mfma_f32_16x16x32_f16 v[148:151], v[56:59], v[216:219], v[24:27]
	v_cvt_pk_f16_f32 v176, |v116|, |v117|
	v_cvt_pk_f16_f32 v177, |v118|, |v119|
	v_mfma_f32_16x16x32_f16 v[188:191], v[72:75], v[172:175], v[188:191]
	v_mfma_f32_16x16x32_f16 v[152:155], v[60:63], v[216:219], v[28:31]
	v_cvt_pk_f16_f32 v178, |v120|, |v121|
	v_cvt_pk_f16_f32 v179, |v122|, |v123|
	v_mfma_f32_16x16x32_f16 v[156:159], v[56:59], v[220:223], v[24:27]
	v_cvt_pk_f16_f32 v180, |v124|, |v125|
	v_cvt_pk_f16_f32 v181, |v126|, |v127|
	v_mfma_f32_16x16x32_f16 v[192:195], v[72:75], v[176:179], v[192:195]
	v_mfma_f32_16x16x32_f16 v[160:163], v[60:63], v[220:223], v[28:31]
	v_cvt_pk_f16_f32 v182, |v128|, |v129|
	v_cvt_pk_f16_f32 v183, |v130|, |v131|
	v_mfma_f32_16x16x32_f16 v[164:167], v[56:59], v[224:227], v[24:27]
	v_cvt_pk_f16_f32 v184, |v132|, |v133|
	v_cvt_pk_f16_f32 v185, |v134|, |v135|
	v_mfma_f32_16x16x32_f16 v[196:199], v[72:75], v[180:183], v[196:199]
	v_mfma_f32_16x16x32_f16 v[168:171], v[60:63], v[224:227], v[28:31]
	v_cvt_pk_f16_f32 v186, |v136|, |v137|
	v_cvt_pk_f16_f32 v187, |v138|, |v139|
	s_nop 1
	v_mfma_f32_16x16x32_f16 v[200:203], v[72:75], v[184:187], v[200:203]
	v_cvt_pk_f16_f32 v172, |v140|, |v141|
	v_cvt_pk_f16_f32 v173, |v142|, |v143|
	v_cvt_pk_f16_f32 v174, |v144|, |v145|
	v_cvt_pk_f16_f32 v175, |v146|, |v147|
	v_cvt_pk_f16_f32 v176, |v148|, |v149|
	v_cvt_pk_f16_f32 v177, |v150|, |v151|
	v_cvt_pk_f16_f32 v178, |v152|, |v153|
	v_cvt_pk_f16_f32 v179, |v154|, |v155|
	v_mfma_f32_16x16x32_f16 v[188:191], v[76:79], v[172:175], v[188:191]
	ds_read2st64_b32 v[100:101], v105 offset1:1
	ds_read2st64_b32 v[98:99], v105 offset0:2 offset1:3
	v_cvt_pk_f16_f32 v180, |v156|, |v157|
	v_cvt_pk_f16_f32 v181, |v158|, |v159|
	v_cvt_pk_f16_f32 v182, |v160|, |v161|
	v_cvt_pk_f16_f32 v183, |v162|, |v163|
	v_mfma_f32_16x16x32_f16 v[192:195], v[76:79], v[176:179], v[192:195]
	v_cvt_pk_f16_f32 v184, |v164|, |v165|
	v_cvt_pk_f16_f32 v185, |v166|, |v167|
	v_cvt_pk_f16_f32 v186, |v168|, |v169|
	v_cvt_pk_f16_f32 v187, |v170|, |v171|
	v_mfma_f32_16x16x32_f16 v[196:199], v[76:79], v[180:183], v[196:199]
	s_nop 1
	v_mfma_f32_16x16x32_f16 v[200:203], v[76:79], v[184:187], v[200:203]
	s_mov_b32 s23, s24
	v_cndmask_b32_e32 v208, 0, v188, vcc
	s_nop 0
	v_cndmask_b32_e64 v208, v208, v192, s[0:1]
	s_nop 0
	v_cndmask_b32_e64 v208, v208, v196, s[2:3]
	s_nop 4
	v_cndmask_b32_e64 v208, v208, v200, s[4:5]
	s_waitcnt lgkmcnt(0)
	v_add_f32_e32 v208, v209, v208
	v_mul_f32_e32 v208, 0xbfb8aa3b, v208
	v_exp_f32_e32 v208, v208
	s_nop 0
	v_add_f32_e32 v208, 1.0, v208
	v_rcp_f32_e32 v208, v208
	s_nop 0
	global_store_dword v[106:107], v208, off sc0 sc1
	s_waitcnt vmcnt(1)
	s_cmp_le_u32 s23, s19
	s_cbranch_scc1 .LBB2_2

	.amdhsa_kernel _Z5k_decPKiPKDF16_S2_PKfS4_S4_Pf
		.amdhsa_group_segment_fixed_size 32768
		.amdhsa_private_segment_fixed_size 0
		.amdhsa_kernarg_size 312
		.amdhsa_user_sgpr_count 2
		.amdhsa_user_sgpr_dispatch_ptr 0
		.amdhsa_user_sgpr_queue_ptr 0
		.amdhsa_user_sgpr_kernarg_segment_ptr 1
		.amdhsa_user_sgpr_dispatch_id 0
		.amdhsa_user_sgpr_kernarg_preload_length 0
		.amdhsa_user_sgpr_kernarg_preload_offset 0
		.amdhsa_user_sgpr_private_segment_size 0
		.amdhsa_uses_dynamic_stack 0
		.amdhsa_enable_private_segment 0
		.amdhsa_system_sgpr_workgroup_id_x 1
		.amdhsa_system_sgpr_workgroup_id_y 0
		.amdhsa_system_sgpr_workgroup_id_z 0
		.amdhsa_system_sgpr_workgroup_info 0
		.amdhsa_system_vgpr_workitem_id 0
		.amdhsa_next_free_vgpr 256
		.amdhsa_next_free_sgpr 96
		.amdhsa_accum_offset 256
		.amdhsa_reserve_vcc 1
		.amdhsa_float_round_mode_32 0
		.amdhsa_float_round_mode_16_64 0
		.amdhsa_float_denorm_mode_32 3
		.amdhsa_float_denorm_mode_16_64 3
		.amdhsa_dx10_clamp 1
		.amdhsa_ieee_mode 1
		.amdhsa_fp16_overflow 0
		.amdhsa_tg_split 0
		.amdhsa_exception_fp_ieee_invalid_op 0
		.amdhsa_exception_fp_denorm_src 0
		.amdhsa_exception_fp_ieee_div_zero 0
		.amdhsa_exception_fp_ieee_overflow 0
		.amdhsa_exception_fp_ieee_underflow 0
		.amdhsa_exception_fp_ieee_inexact 0
		.amdhsa_exception_int_div_zero 0
	.end_amdhsa_kernel

amdhsa.kernels:
  - .agpr_count:     0
    .args:
      - .actual_access:  read_only
        .address_space:  global
        .offset:         0
        .size:           8
        .value_kind:     global_buffer
      - .actual_access:  read_only
        .address_space:  global
        .offset:         8
        .size:           8
        .value_kind:     global_buffer
      - .actual_access:  write_only
        .address_space:  global
        .offset:         16
        .size:           8
        .value_kind:     global_buffer
      - .actual_access:  read_only
        .address_space:  global
        .offset:         24
        .size:           8
        .value_kind:     global_buffer
      - .actual_access:  write_only
        .address_space:  global
        .offset:         32
        .size:           8
        .value_kind:     global_buffer
      - .actual_access:  write_only
        .address_space:  global
        .offset:         40
        .size:           8
        .value_kind:     global_buffer
      - .actual_access:  read_only
        .address_space:  global
        .offset:         48
        .size:           8
        .value_kind:     global_buffer
      - .actual_access:  read_only
        .address_space:  global
        .offset:         56
        .size:           8
        .value_kind:     global_buffer
      - .actual_access:  write_only
        .address_space:  global
        .offset:         64
        .size:           8
        .value_kind:     global_buffer
    .group_segment_fixed_size: 53904
    .kernarg_segment_align: 8
    .kernarg_segment_size: 72
    .language:       OpenCL C
    .language_version:
      - 2
      - 0
    .max_flat_workgroup_size: 1024
    .name:           _Z6k_partPKiS0_PiS1_PjS1_PKfS4_Pf
    .private_segment_fixed_size: 0
    .sgpr_count:     31
    .sgpr_spill_count: 0
    .symbol:         _Z6k_partPKiS0_PiS1_PjS1_PKfS4_Pf.kd
    .uniform_work_group_size: 1
    .uses_dynamic_stack: false
    .vgpr_count:     64
    .vgpr_spill_count: 0
    .wavefront_size: 64
  - .agpr_count:     0
    .args:
      - .actual_access:  read_only
        .address_space:  global
        .offset:         0
        .size:           8
        .value_kind:     global_buffer
      - .actual_access:  read_only
        .address_space:  global
        .offset:         8
        .size:           8
        .value_kind:     global_buffer
      - .actual_access:  read_only
        .address_space:  global
        .offset:         16
        .size:           8
        .value_kind:     global_buffer
      - .address_space:  global
        .offset:         24
        .size:           8
        .value_kind:     global_buffer
      - .actual_access:  read_only
        .address_space:  global
        .offset:         32
        .size:           8
        .value_kind:     global_buffer
      - .actual_access:  write_only
        .address_space:  global
        .offset:         40
        .size:           8
        .value_kind:     global_buffer
      - .actual_access:  write_only
        .address_space:  global
        .offset:         48
        .size:           8
        .value_kind:     global_buffer
      - .actual_access:  write_only
        .address_space:  global
        .offset:         56
        .size:           8
        .value_kind:     global_buffer
      - .actual_access:  write_only
        .address_space:  global
        .offset:         64
        .size:           8
        .value_kind:     global_buffer
      - .actual_access:  write_only
        .address_space:  global
        .offset:         72
        .size:           8
        .value_kind:     global_buffer
      - .actual_access:  read_only
        .address_space:  global
        .offset:         80
        .size:           8
        .value_kind:     global_buffer
      - .actual_access:  read_only
        .address_space:  global
        .offset:         88
        .size:           8
        .value_kind:     global_buffer
      - .actual_access:  read_only
        .address_space:  global
        .offset:         96
        .size:           8
        .value_kind:     global_buffer
      - .actual_access:  read_only
        .address_space:  global
        .offset:         104
        .size:           8
        .value_kind:     global_buffer
      - .actual_access:  write_only
        .address_space:  global
        .offset:         112
        .size:           8
        .value_kind:     global_buffer
      - .actual_access:  write_only
        .address_space:  global
        .offset:         120
        .size:           8
        .value_kind:     global_buffer
    .group_segment_fixed_size: 38940
    .kernarg_segment_align: 8
    .kernarg_segment_size: 128
    .language:       OpenCL C
    .language_version:
      - 2
      - 0
    .max_flat_workgroup_size: 1024
    .name:           _Z5k_csrPKjPKiS2_PiPKfPfPDF16_S3_S3_S3_S5_S5_S5_S5_S7_S6_
    .private_segment_fixed_size: 0
    .sgpr_count:     72
    .sgpr_spill_count: 0
    .symbol:         _Z5k_csrPKjPKiS2_PiPKfPfPDF16_S3_S3_S3_S5_S5_S5_S5_S7_S6_.kd
    .uniform_work_group_size: 1
    .uses_dynamic_stack: false
    .vgpr_count:     64
    .vgpr_spill_count: 0
    .wavefront_size: 64
  - .agpr_count:     0
    .args:
      - .actual_access:  read_only
        .address_space:  global
        .offset:         0
        .size:           8
        .value_kind:     global_buffer
      - .actual_access:  read_only
        .address_space:  global
        .offset:         8
        .size:           8
        .value_kind:     global_buffer
      - .actual_access:  read_only
        .address_space:  global
        .offset:         16
        .size:           8
        .value_kind:     global_buffer
      - .actual_access:  read_only
        .address_space:  global
        .offset:         24
        .size:           8
        .value_kind:     global_buffer
      - .actual_access:  read_only
        .address_space:  global
        .offset:         32
        .size:           8
        .value_kind:     global_buffer
      - .actual_access:  read_only
        .address_space:  global
        .offset:         40
        .size:           8
        .value_kind:     global_buffer
      - .actual_access:  write_only
        .address_space:  global
        .offset:         48
        .size:           8
        .value_kind:     global_buffer
      - .offset:         56
        .size:           4
        .value_kind:     hidden_block_count_x
      - .offset:         60
        .size:           4
        .value_kind:     hidden_block_count_y
      - .offset:         64
        .size:           4
        .value_kind:     hidden_block_count_z
      - .offset:         68
        .size:           2
        .value_kind:     hidden_group_size_x
      - .offset:         70
        .size:           2
        .value_kind:     hidden_group_size_y
      - .offset:         72
        .size:           2
        .value_kind:     hidden_group_size_z
      - .offset:         74
        .size:           2
        .value_kind:     hidden_remainder_x
      - .offset:         76
        .size:           2
        .value_kind:     hidden_remainder_y
      - .offset:         78
        .size:           2
        .value_kind:     hidden_remainder_z
      - .offset:         96
        .size:           8
        .value_kind:     hidden_global_offset_x
      - .offset:         104
        .size:           8
        .value_kind:     hidden_global_offset_y
      - .offset:         112
        .size:           8
        .value_kind:     hidden_global_offset_z
      - .offset:         120
        .size:           2
        .value_kind:     hidden_grid_dims
    .group_segment_fixed_size: 32768
    .kernarg_segment_align: 8
    .kernarg_segment_size: 312
    .language:       OpenCL C
    .language_version:
      - 2
      - 0
    .max_flat_workgroup_size: 256
    .name:           _Z5k_decPKiPKDF16_S2_PKfS4_S4_Pf
    .private_segment_fixed_size: 0
    .sgpr_count:     28
    .sgpr_spill_count: 0
    .symbol:         _Z5k_decPKiPKDF16_S2_PKfS4_S4_Pf.kd
    .uniform_work_group_size: 1
    .uses_dynamic_stack: false
    .vgpr_count:     256
    .vgpr_spill_count: 0
    .wavefront_size: 64
  - .agpr_count:     0
    .args:
      - .actual_access:  read_only
        .address_space:  global
        .offset:         0
        .size:           8
        .value_kind:     global_buffer
      - .actual_access:  read_only
        .address_space:  global
        .offset:         8
        .size:           8
        .value_kind:     global_buffer
      - .actual_access:  read_only
        .address_space:  global
        .offset:         16
        .size:           8
        .value_kind:     global_buffer
      - .actual_access:  read_only
        .address_space:  global
        .offset:         24
        .size:           8
        .value_kind:     global_buffer
      - .actual_access:  read_only
        .address_space:  global
        .offset:         32
        .size:           8
        .value_kind:     global_buffer
      - .actual_access:  read_only
        .address_space:  global
        .offset:         40
        .size:           8
        .value_kind:     global_buffer
      - .actual_access:  write_only
        .address_space:  global
        .offset:         48
        .size:           8
        .value_kind:     global_buffer
      - .actual_access:  read_only
        .address_space:  global
        .offset:         56
        .size:           8
        .value_kind:     global_buffer
    .group_segment_fixed_size: 0
    .kernarg_segment_align: 8
    .kernarg_segment_size: 64
    .language:       OpenCL C
    .language_version:
      - 2
      - 0
    .max_flat_workgroup_size: 64
    .name:           _Z5k_aggILi1EEvPKiS1_S1_PKDv4_jPKfS6_PS2_PDF16_
    .private_segment_fixed_size: 0
    .sgpr_count:     82
    .sgpr_spill_count: 0
    .symbol:         _Z5k_aggILi1EEvPKiS1_S1_PKDv4_jPKfS6_PS2_PDF16_.kd
    .uniform_work_group_size: 1
    .uses_dynamic_stack: false
    .vgpr_count:     72
    .vgpr_spill_count: 0
    .wavefront_size: 64
  - .agpr_count:     0
    .args:
      - .actual_access:  read_only
        .address_space:  global
        .offset:         0
        .size:           8
        .value_kind:     global_buffer
      - .actual_access:  read_only
        .address_space:  global
        .offset:         8
        .size:           8
        .value_kind:     global_buffer
      - .actual_access:  read_only
        .address_space:  global
        .offset:         16
        .size:           8
        .value_kind:     global_buffer
      - .actual_access:  read_only
        .address_space:  global
        .offset:         24
        .size:           8
        .value_kind:     global_buffer
      - .actual_access:  read_only
        .address_space:  global
        .offset:         32
        .size:           8
        .value_kind:     global_buffer
      - .actual_access:  read_only
        .address_space:  global
        .offset:         40
        .size:           8
        .value_kind:     global_buffer
      - .actual_access:  read_only
        .address_space:  global
        .offset:         48
        .size:           8
        .value_kind:     global_buffer
      - .actual_access:  write_only
        .address_space:  global
        .offset:         56
        .size:           8
        .value_kind:     global_buffer
    .group_segment_fixed_size: 0
    .kernarg_segment_align: 8
    .kernarg_segment_size: 64
    .language:       OpenCL C
    .language_version:
      - 2
      - 0
    .max_flat_workgroup_size: 64
    .name:           _Z5k_aggILi2EEvPKiS1_S1_PKDv4_jPKfS6_PS2_PDF16_
    .private_segment_fixed_size: 0
    .sgpr_count:     66
    .sgpr_spill_count: 0
    .symbol:         _Z5k_aggILi2EEvPKiS1_S1_PKDv4_jPKfS6_PS2_PDF16_.kd
    .uniform_work_group_size: 1
    .uses_dynamic_stack: false
    .vgpr_count:     72
    .vgpr_spill_count: 0
    .wavefront_size: 64
